# baseline (speedup 1.0000x reference)
.LBB1_122:
	s_mov_b32 s2, 0xfd000000
	v_cmp_eq_u32_e64 s[0:1], 0, v0
	s_waitcnt vmcnt(19)
	v_mov_b32_e32 v3, 0
	v_mov_b32_e32 v1, 0x24820
	s_movk_i32 s12, 0x23f
	s_movk_i32 s13, 0x1800
	s_mov_b32 s14, 0x300000
	s_mov_b32 s3, -1
	s_mov_b32 s15, 0x2ffe00
	s_mov_b64 s[4:5], 0x2000
	s_and_saveexec_b64 s[8:9], s[0:1]
	s_cbranch_execz .Lcv_skip1
	v_mov_b32_e32 v100, 1
	global_atomic_add v100, v3, v100, s[74:75] sc0
.Lcv_skip1:
	s_or_b64 exec, exec, s[8:9]
	s_branch .LBB1_124

.LBB1_124:
	s_and_saveexec_b64 s[6:7], s[0:1]
	s_cbranch_execz .LBB1_128
	s_waitcnt vmcnt(0)
	ds_write_b32 v1, v100
.LBB1_128:
	s_or_b64 exec, exec, s[6:7]
	s_waitcnt lgkmcnt(0)
	s_barrier
	ds_read_b32 v2, v1
	s_mov_b64 s[6:7], -1
	s_waitcnt lgkmcnt(0)
	s_barrier
	v_cmp_lt_i32_e32 vcc, s12, v2
	s_cbranch_vccnz .LBB1_123
	s_and_saveexec_b64 s[8:9], s[0:1]
	s_cbranch_execz .Lcv_skip2
	v_mov_b32_e32 v100, 1
	global_atomic_add v100, v3, v100, s[74:75] sc0
.Lcv_skip2:
	s_or_b64 exec, exec, s[8:9]
	v_mul_lo_u32 v2, v2, s13
	v_or_b32_e32 v52, v2, v0
	v_mov_b32_e32 v2, v52
	v_or_b32_e32 v54, 0x200, v52
	v_ashrrev_i32_e32 v53, 31, v52
	v_lshl_add_u64 v[4:5], v[2:3], 4, s[72:73]
	v_mov_b32_e32 v2, v54
	v_or_b32_e32 v56, 0x400, v52
	s_waitcnt vmcnt(18)
	v_lshl_add_u64 v[8:9], v[52:53], 4, s[70:71]
	v_lshl_add_u64 v[4:5], v[4:5], 0, s[2:3]
	v_cmp_gt_i32_e32 vcc, s14, v52
	s_waitcnt vmcnt(17)
	v_lshl_add_u64 v[10:11], v[2:3], 4, s[72:73]
	v_mov_b32_e32 v2, v56
	v_or_b32_e32 v58, 0x600, v52
	v_cndmask_b32_e32 v5, v5, v9, vcc
	v_cndmask_b32_e32 v4, v4, v8, vcc
	v_lshl_add_u64 v[8:9], v[8:9], 0, s[4:5]
	v_lshl_add_u64 v[10:11], v[10:11], 0, s[2:3]
	v_cmp_gt_i32_e32 vcc, s15, v52
	v_ashrrev_i32_e32 v57, 31, v56
	s_waitcnt vmcnt(16)
	v_lshl_add_u64 v[14:15], v[2:3], 4, s[72:73]
	v_mov_b32_e32 v2, v58
	v_add_u32_e32 v60, 0x800, v52
	global_load_dwordx4 v[4:7], v[4:5], off nt
	v_cndmask_b32_e32 v9, v11, v9, vcc
	v_cndmask_b32_e32 v8, v10, v8, vcc
	v_lshl_add_u64 v[12:13], v[56:57], 4, s[70:71]
	v_lshl_add_u64 v[14:15], v[14:15], 0, s[2:3]
	v_cmp_gt_i32_e32 vcc, s14, v56
	v_ashrrev_i32_e32 v59, 31, v58
	s_waitcnt vmcnt(15)
	v_lshl_add_u64 v[18:19], v[2:3], 4, s[72:73]
	v_mov_b32_e32 v2, v60
	v_add_u32_e32 v62, 0xa00, v52
	global_load_dwordx4 v[8:11], v[8:9], off nt
	v_cndmask_b32_e32 v13, v15, v13, vcc
	v_cndmask_b32_e32 v12, v14, v12, vcc
	v_lshl_add_u64 v[16:17], v[58:59], 4, s[70:71]
	v_lshl_add_u64 v[18:19], v[18:19], 0, s[2:3]
	v_cmp_gt_i32_e32 vcc, s14, v58
	v_ashrrev_i32_e32 v61, 31, v60
	v_lshl_add_u64 v[22:23], v[2:3], 4, s[72:73]
	v_mov_b32_e32 v2, v62
	v_add_u32_e32 v64, 0xc00, v52
	global_load_dwordx4 v[12:15], v[12:13], off nt
	v_cndmask_b32_e32 v17, v19, v17, vcc
	v_cndmask_b32_e32 v16, v18, v16, vcc
	v_lshl_add_u64 v[20:21], v[60:61], 4, s[70:71]
	v_lshl_add_u64 v[22:23], v[22:23], 0, s[2:3]
	v_cmp_gt_i32_e32 vcc, s14, v60
	v_ashrrev_i32_e32 v63, 31, v62
	s_waitcnt vmcnt(15)
	v_lshl_add_u64 v[26:27], v[2:3], 4, s[72:73]
	v_mov_b32_e32 v2, v64
	v_add_u32_e32 v66, 0xe00, v52
	global_load_dwordx4 v[16:19], v[16:17], off nt
	v_cndmask_b32_e32 v21, v23, v21, vcc
	v_cndmask_b32_e32 v20, v22, v20, vcc
	v_lshl_add_u64 v[24:25], v[62:63], 4, s[70:71]
	v_lshl_add_u64 v[26:27], v[26:27], 0, s[2:3]
	v_cmp_gt_i32_e32 vcc, s14, v62
	v_ashrrev_i32_e32 v65, 31, v64
	v_lshl_add_u64 v[30:31], v[2:3], 4, s[72:73]
	v_mov_b32_e32 v2, v66
	v_add_u32_e32 v68, 0x1000, v52
	global_load_dwordx4 v[20:23], v[20:21], off nt
	v_cndmask_b32_e32 v25, v27, v25, vcc
	v_cndmask_b32_e32 v24, v26, v24, vcc
	v_lshl_add_u64 v[28:29], v[64:65], 4, s[70:71]
	v_lshl_add_u64 v[30:31], v[30:31], 0, s[2:3]
	v_cmp_gt_i32_e32 vcc, s14, v64
	v_ashrrev_i32_e32 v67, 31, v66
	s_waitcnt vmcnt(15)
	v_lshl_add_u64 v[34:35], v[2:3], 4, s[72:73]
	v_mov_b32_e32 v2, v68
	v_add_u32_e32 v70, 0x1200, v52
	global_load_dwordx4 v[24:27], v[24:25], off nt
	v_cndmask_b32_e32 v29, v31, v29, vcc
	v_cndmask_b32_e32 v28, v30, v28, vcc
	v_lshl_add_u64 v[32:33], v[66:67], 4, s[70:71]
	v_lshl_add_u64 v[34:35], v[34:35], 0, s[2:3]
	v_cmp_gt_i32_e32 vcc, s14, v66
	v_ashrrev_i32_e32 v69, 31, v68
	v_lshl_add_u64 v[38:39], v[2:3], 4, s[72:73]
	v_mov_b32_e32 v2, v70
	v_add_u32_e32 v72, 0x1400, v52
	global_load_dwordx4 v[28:31], v[28:29], off nt
	v_cndmask_b32_e32 v33, v35, v33, vcc
	v_cndmask_b32_e32 v32, v34, v32, vcc
	v_lshl_add_u64 v[36:37], v[68:69], 4, s[70:71]
	v_lshl_add_u64 v[38:39], v[38:39], 0, s[2:3]
	v_cmp_gt_i32_e32 vcc, s14, v68
	v_ashrrev_i32_e32 v71, 31, v70
	s_waitcnt vmcnt(15)
	v_lshl_add_u64 v[42:43], v[2:3], 4, s[72:73]
	v_mov_b32_e32 v2, v72
	v_add_u32_e32 v74, 0x1600, v52
	global_load_dwordx4 v[32:35], v[32:33], off nt
	v_cndmask_b32_e32 v37, v39, v37, vcc
	v_cndmask_b32_e32 v36, v38, v36, vcc
	v_lshl_add_u64 v[40:41], v[70:71], 4, s[70:71]
	v_lshl_add_u64 v[42:43], v[42:43], 0, s[2:3]
	v_cmp_gt_i32_e32 vcc, s14, v70
	v_ashrrev_i32_e32 v73, 31, v72
	v_lshl_add_u64 v[46:47], v[2:3], 4, s[72:73]
	v_mov_b32_e32 v2, v74
	global_load_dwordx4 v[36:39], v[36:37], off nt
	v_cndmask_b32_e32 v41, v43, v41, vcc
	v_cndmask_b32_e32 v40, v42, v40, vcc
	v_lshl_add_u64 v[44:45], v[72:73], 4, s[70:71]
	v_lshl_add_u64 v[46:47], v[46:47], 0, s[2:3]
	v_cmp_gt_i32_e32 vcc, s14, v72
	v_ashrrev_i32_e32 v75, 31, v74
	v_lshl_add_u64 v[50:51], v[2:3], 4, s[72:73]
	global_load_dwordx4 v[40:43], v[40:41], off nt
	v_cndmask_b32_e32 v45, v47, v45, vcc
	v_cndmask_b32_e32 v44, v46, v44, vcc
	v_lshl_add_u64 v[48:49], v[74:75], 4, s[70:71]
	v_lshl_add_u64 v[50:51], v[50:51], 0, s[2:3]
	v_cmp_gt_i32_e32 vcc, s14, v74
	global_load_dwordx4 v[44:47], v[44:45], off nt
	v_ashrrev_i32_e32 v55, 31, v54
	v_cndmask_b32_e32 v49, v51, v49, vcc
	v_cndmask_b32_e32 v48, v50, v48, vcc
	global_load_dwordx4 v[48:51], v[48:49], off nt
	s_waitcnt vmcnt(11)
	v_cvt_pk_f16_f32 v7, v6, v7
	v_cvt_pk_f16_f32 v6, v4, v5
	v_lshl_add_u64 v[4:5], v[52:53], 3, s[68:69]
	global_store_dwordx2 v[4:5], v[6:7], off
	s_waitcnt vmcnt(11)
	v_cvt_pk_f16_f32 v5, v10, v11
	v_cvt_pk_f16_f32 v4, v8, v9
	v_lshl_add_u64 v[6:7], v[54:55], 3, s[68:69]
	global_store_dwordx2 v[6:7], v[4:5], off
	s_waitcnt vmcnt(11)
	v_cvt_pk_f16_f32 v5, v14, v15
	v_cvt_pk_f16_f32 v4, v12, v13
	v_lshl_add_u64 v[6:7], v[56:57], 3, s[68:69]
	global_store_dwordx2 v[6:7], v[4:5], off
	s_waitcnt vmcnt(11)
	v_cvt_pk_f16_f32 v5, v18, v19
	v_cvt_pk_f16_f32 v4, v16, v17
	v_lshl_add_u64 v[6:7], v[58:59], 3, s[68:69]
	global_store_dwordx2 v[6:7], v[4:5], off
	v_lshl_add_u64 v[6:7], v[60:61], 3, s[68:69]
	s_mov_b64 s[6:7], 0
	s_waitcnt vmcnt(11)
	v_cvt_pk_f16_f32 v5, v22, v23
	v_cvt_pk_f16_f32 v4, v20, v21
	global_store_dwordx2 v[6:7], v[4:5], off
	v_lshl_add_u64 v[6:7], v[62:63], 3, s[68:69]
	s_waitcnt vmcnt(11)
	v_cvt_pk_f16_f32 v5, v26, v27
	v_cvt_pk_f16_f32 v4, v24, v25
	global_store_dwordx2 v[6:7], v[4:5], off
	v_lshl_add_u64 v[6:7], v[64:65], 3, s[68:69]
	s_waitcnt vmcnt(11)
	v_cvt_pk_f16_f32 v5, v30, v31
	v_cvt_pk_f16_f32 v4, v28, v29
	global_store_dwordx2 v[6:7], v[4:5], off
	v_lshl_add_u64 v[6:7], v[66:67], 3, s[68:69]
	s_waitcnt vmcnt(11)
	v_cvt_pk_f16_f32 v5, v34, v35
	v_cvt_pk_f16_f32 v4, v32, v33
	global_store_dwordx2 v[6:7], v[4:5], off
	v_lshl_add_u64 v[6:7], v[68:69], 3, s[68:69]
	s_waitcnt vmcnt(11)
	v_cvt_pk_f16_f32 v5, v38, v39
	v_cvt_pk_f16_f32 v4, v36, v37
	global_store_dwordx2 v[6:7], v[4:5], off
	v_lshl_add_u64 v[6:7], v[70:71], 3, s[68:69]
	s_waitcnt vmcnt(11)
	v_cvt_pk_f16_f32 v5, v42, v43
	v_cvt_pk_f16_f32 v4, v40, v41
	global_store_dwordx2 v[6:7], v[4:5], off
	v_lshl_add_u64 v[6:7], v[72:73], 3, s[68:69]
	s_waitcnt vmcnt(11)
	v_cvt_pk_f16_f32 v5, v46, v47
	v_cvt_pk_f16_f32 v4, v44, v45
	global_store_dwordx2 v[6:7], v[4:5], off
	v_lshl_add_u64 v[6:7], v[74:75], 3, s[68:69]
	s_waitcnt vmcnt(11)
	v_cvt_pk_f16_f32 v5, v50, v51
	v_cvt_pk_f16_f32 v4, v48, v49
	global_store_dwordx2 v[6:7], v[4:5], off
	s_branch .LBB1_123
